# P3 merge epilogue: 10 of 16 gate loads per pass prefetched inside the last K-loop iteration into free VGPRs, rest batched
# baseline (speedup 1.0000x reference)
.LBB0_563:
	v_add_u32_e32 v3, 0x10000, v209
	ds_read_b128 v[140:143], v3
	ds_read_b128 v[144:147], v3 offset:1024
	ds_read_b128 v[148:151], v3 offset:2048
	ds_read_b128 v[152:155], v3 offset:3072
	v_add_u32_e32 v3, 0x14000, v209
	ds_read_b128 v[156:159], v3
	ds_read_b128 v[160:163], v3 offset:1024
	ds_read_b128 v[164:167], v3 offset:2048
	ds_read_b128 v[168:171], v3 offset:3072
	s_add_i32 s10, s57, 0xfff80080
	s_cmp_eq_u32 s59, 12
	s_cselect_b32 s62, s2, s10
	s_cselect_b32 s61, s3, s58
	s_add_i32 s60, s62, 0x80
	s_mov_b32 m0, s44
	ds_read_b128 v[172:175], v210
	ds_read_b128 v[176:179], v210 offset:1024
	ds_read_b128 v[180:183], v210 offset:2048
	ds_read_b128 v[184:187], v210 offset:3072
	ds_read_b128 v[188:191], v210 offset:4096
	ds_read_b128 v[192:195], v210 offset:5120
	ds_read_b128 v[196:199], v210 offset:6144
	ds_read_b128 v[200:203], v210 offset:7168
	buffer_load_dwordx4 v1, s[4:7], s57 offen lds
	s_mov_b32 m0, s45
	s_nop 0
	buffer_load_dwordx4 v206, s[4:7], s57 offen lds
	s_waitcnt vmcnt(8)
	s_waitcnt lgkmcnt(0)
	s_cmp_eq_u32 s59, 12
	s_cbranch_scc0 .Lp3_nopf
	s_lshl_b32 s98, s22, 8
	v_lshl_add_u32 v252, s23, 8, v208
	s_ashr_i32 s99, s98, 31
	v_ashrrev_i32_e32 v253, 31, v252
	v_lshlrev_b64 v[252:253], 11, v[252:253]
	v_lshl_add_u64 v[252:253], v[252:253], 0, s[98:99]
	s_cmp_eq_u32 s56, 0
	s_cselect_b32 s98, s46, 0x11b00000
	v_readlane_b32 s100, v255, 3
	v_readlane_b32 s101, v255, 4
	s_add_u32 s100, s100, s98
	v_or_b32_e32 v252, v252, v134
	s_addc_u32 s101, s101, 0
	v_lshl_add_u64 v[252:253], v[252:253], 1, s[100:101]
	v_add_co_u32_e32 v204, vcc, 0x20000, v252
	s_nop 1
	v_addc_co_u32_e32 v205, vcc, 0, v253, vcc
	global_load_dwordx4 v[212:215], v[204:205], off offset:256 nt
	v_add_co_u32_e32 v204, vcc, 0x30000, v252
	s_nop 1
	v_addc_co_u32_e32 v205, vcc, 0, v253, vcc
	global_load_dwordx4 v[216:219], v[204:205], off nt
	global_load_dwordx4 v[220:223], v[204:205], off offset:256 nt
	v_add_co_u32_e32 v204, vcc, 0x80000, v252
	s_nop 1
	v_addc_co_u32_e32 v205, vcc, 0, v253, vcc
	global_load_dwordx4 v[224:227], v[204:205], off nt
	global_load_dwordx4 v[228:231], v[204:205], off offset:256 nt
	v_add_co_u32_e32 v204, vcc, 0x90000, v252
	s_nop 1
	v_addc_co_u32_e32 v205, vcc, 0, v253, vcc
	global_load_dwordx4 v[232:235], v[204:205], off nt
	global_load_dwordx4 v[236:239], v[204:205], off offset:256 nt
	v_add_co_u32_e32 v204, vcc, 0xa0000, v252
	s_nop 1
	v_addc_co_u32_e32 v205, vcc, 0, v253, vcc
	global_load_dwordx4 v[240:243], v[204:205], off nt
	global_load_dwordx4 v[244:247], v[204:205], off offset:256 nt
	v_add_co_u32_e32 v204, vcc, 0xb0000, v252
	s_nop 1
	v_addc_co_u32_e32 v205, vcc, 0, v253, vcc
	global_load_dwordx4 v[248:251], v[204:205], off nt
.Lp3_nopf:
	s_barrier
	s_setprio 1
	s_waitcnt lgkmcnt(7)
	v_mfma_f32_16x16x32_bf16 v[130:133], v[140:143], v[172:175], v[130:133]
	v_mfma_f32_16x16x32_bf16 v[126:129], v[148:151], v[172:175], v[126:129]
	s_waitcnt lgkmcnt(5)
	v_mfma_f32_16x16x32_bf16 v[122:125], v[140:143], v[180:183], v[122:125]
	v_mfma_f32_16x16x32_bf16 v[118:121], v[148:151], v[180:183], v[118:121]
	s_waitcnt lgkmcnt(3)
	v_mfma_f32_16x16x32_bf16 v[114:117], v[140:143], v[188:191], v[114:117]
	v_mfma_f32_16x16x32_bf16 v[110:113], v[148:151], v[188:191], v[110:113]
	s_waitcnt lgkmcnt(1)
	v_mfma_f32_16x16x32_bf16 v[106:109], v[140:143], v[196:199], v[106:109]
	v_mfma_f32_16x16x32_bf16 v[102:105], v[148:151], v[196:199], v[102:105]
	v_mfma_f32_16x16x32_bf16 v[130:133], v[144:147], v[176:179], v[130:133]
	v_mfma_f32_16x16x32_bf16 v[126:129], v[152:155], v[176:179], v[126:129]
	v_mfma_f32_16x16x32_bf16 v[122:125], v[144:147], v[184:187], v[122:125]
	v_mfma_f32_16x16x32_bf16 v[118:121], v[152:155], v[184:187], v[118:121]
	v_mfma_f32_16x16x32_bf16 v[114:117], v[144:147], v[192:195], v[114:117]
	v_mfma_f32_16x16x32_bf16 v[110:113], v[152:155], v[192:195], v[110:113]
	s_waitcnt lgkmcnt(0)
	v_mfma_f32_16x16x32_bf16 v[106:109], v[144:147], v[200:203], v[106:109]
	v_mfma_f32_16x16x32_bf16 v[102:105], v[152:155], v[200:203], v[102:105]
	s_setprio 0
	s_setprio 1
	v_mfma_f32_16x16x32_bf16 v[98:101], v[156:159], v[172:175], v[98:101]
	v_mfma_f32_16x16x32_bf16 v[94:97], v[164:167], v[172:175], v[94:97]
	v_mfma_f32_16x16x32_bf16 v[90:93], v[156:159], v[180:183], v[90:93]
	v_mfma_f32_16x16x32_bf16 v[86:89], v[164:167], v[180:183], v[86:89]
	v_mfma_f32_16x16x32_bf16 v[82:85], v[156:159], v[188:191], v[82:85]
	v_mfma_f32_16x16x32_bf16 v[78:81], v[164:167], v[188:191], v[78:81]
	v_mfma_f32_16x16x32_bf16 v[74:77], v[156:159], v[196:199], v[74:77]
	v_mfma_f32_16x16x32_bf16 v[70:73], v[164:167], v[196:199], v[70:73]
	v_mfma_f32_16x16x32_bf16 v[98:101], v[160:163], v[176:179], v[98:101]
	v_mfma_f32_16x16x32_bf16 v[94:97], v[168:171], v[176:179], v[94:97]
	v_mfma_f32_16x16x32_bf16 v[90:93], v[160:163], v[184:187], v[90:93]
	v_mfma_f32_16x16x32_bf16 v[86:89], v[168:171], v[184:187], v[86:89]
	v_mfma_f32_16x16x32_bf16 v[82:85], v[160:163], v[192:195], v[82:85]
	v_mfma_f32_16x16x32_bf16 v[78:81], v[168:171], v[192:195], v[78:81]
	v_mfma_f32_16x16x32_bf16 v[74:77], v[160:163], v[200:203], v[74:77]
	v_mfma_f32_16x16x32_bf16 v[70:73], v[168:171], v[200:203], v[70:73]
	s_setprio 0
	s_barrier
	s_mov_b32 m0, s28
	s_mov_b32 s10, s6
	s_mov_b32 s11, s7
	ds_read_b128 v[172:175], v210 offset:16384
	ds_read_b128 v[176:179], v210 offset:17408
	ds_read_b128 v[180:183], v210 offset:18432
	ds_read_b128 v[184:187], v210 offset:19456
	ds_read_b128 v[188:191], v210 offset:20480
	ds_read_b128 v[192:195], v210 offset:21504
	ds_read_b128 v[196:199], v210 offset:22528
	ds_read_b128 v[200:203], v210 offset:23552
	buffer_load_dwordx4 v135, s[8:11], s61 offen lds
	s_mov_b32 m0, s29
	s_add_i32 s63, s61, 0x80000
	buffer_load_dwordx4 v207, s[8:11], s61 offen lds
	s_mov_b32 m0, s30
	s_nop 0
	buffer_load_dwordx4 v135, s[8:11], s63 offen lds
	s_mov_b32 m0, s31
	s_nop 0
	buffer_load_dwordx4 v207, s[8:11], s63 offen lds
	s_mov_b32 m0, s27
	s_nop 0
	buffer_load_dwordx4 v1, s[4:7], s62 offen lds
	s_mov_b32 m0, s33
	s_nop 0
	buffer_load_dwordx4 v206, s[4:7], s62 offen lds
	s_waitcnt vmcnt(8)
	s_waitcnt lgkmcnt(0)
	s_barrier
	s_setprio 1
	s_waitcnt lgkmcnt(7)
	v_mfma_f32_16x16x32_bf16 v[66:69], v[140:143], v[172:175], v[66:69]
	v_mfma_f32_16x16x32_bf16 v[62:65], v[148:151], v[172:175], v[62:65]
	s_waitcnt lgkmcnt(5)
	v_mfma_f32_16x16x32_bf16 v[58:61], v[140:143], v[180:183], v[58:61]
	v_mfma_f32_16x16x32_bf16 v[54:57], v[148:151], v[180:183], v[54:57]
	s_waitcnt lgkmcnt(3)
	v_mfma_f32_16x16x32_bf16 v[50:53], v[140:143], v[188:191], v[50:53]
	v_mfma_f32_16x16x32_bf16 v[46:49], v[148:151], v[188:191], v[46:49]
	s_waitcnt lgkmcnt(1)
	v_mfma_f32_16x16x32_bf16 v[42:45], v[140:143], v[196:199], v[42:45]
	v_mfma_f32_16x16x32_bf16 v[38:41], v[148:151], v[196:199], v[38:41]
	v_mfma_f32_16x16x32_bf16 v[66:69], v[144:147], v[176:179], v[66:69]
	v_mfma_f32_16x16x32_bf16 v[62:65], v[152:155], v[176:179], v[62:65]
	v_mfma_f32_16x16x32_bf16 v[58:61], v[144:147], v[184:187], v[58:61]
	v_mfma_f32_16x16x32_bf16 v[54:57], v[152:155], v[184:187], v[54:57]
	v_mfma_f32_16x16x32_bf16 v[50:53], v[144:147], v[192:195], v[50:53]
	v_mfma_f32_16x16x32_bf16 v[46:49], v[152:155], v[192:195], v[46:49]
	s_waitcnt lgkmcnt(0)
	v_mfma_f32_16x16x32_bf16 v[42:45], v[144:147], v[200:203], v[42:45]
	v_mfma_f32_16x16x32_bf16 v[38:41], v[152:155], v[200:203], v[38:41]
	s_setprio 0
	s_setprio 1
	v_mfma_f32_16x16x32_bf16 v[34:37], v[156:159], v[172:175], v[34:37]
	v_mfma_f32_16x16x32_bf16 v[30:33], v[164:167], v[172:175], v[30:33]
	v_mfma_f32_16x16x32_bf16 v[26:29], v[156:159], v[180:183], v[26:29]
	v_mfma_f32_16x16x32_bf16 v[22:25], v[164:167], v[180:183], v[22:25]
	v_mfma_f32_16x16x32_bf16 v[18:21], v[156:159], v[188:191], v[18:21]
	v_mfma_f32_16x16x32_bf16 v[14:17], v[164:167], v[188:191], v[14:17]
	v_mfma_f32_16x16x32_bf16 v[10:13], v[156:159], v[196:199], v[10:13]
	v_mfma_f32_16x16x32_bf16 v[4:7], v[164:167], v[196:199], v[6:9]
	v_mfma_f32_16x16x32_bf16 v[34:37], v[160:163], v[176:179], v[34:37]
	v_mfma_f32_16x16x32_bf16 v[30:33], v[168:171], v[176:179], v[30:33]
	v_mfma_f32_16x16x32_bf16 v[26:29], v[160:163], v[184:187], v[26:29]
	v_mfma_f32_16x16x32_bf16 v[22:25], v[168:171], v[184:187], v[22:25]
	v_mfma_f32_16x16x32_bf16 v[18:21], v[160:163], v[192:195], v[18:21]
	v_mfma_f32_16x16x32_bf16 v[14:17], v[168:171], v[192:195], v[14:17]
	v_mfma_f32_16x16x32_bf16 v[10:13], v[160:163], v[200:203], v[10:13]
	v_mfma_f32_16x16x32_bf16 v[4:7], v[168:171], v[200:203], v[4:7]
	s_setprio 0
	s_barrier
	v_add_u32_e32 v3, 0x18000, v209
	ds_read_b128 v[140:143], v3
	ds_read_b128 v[144:147], v3 offset:1024
	ds_read_b128 v[148:151], v3 offset:2048
	ds_read_b128 v[152:155], v3 offset:3072
	v_add_u32_e32 v3, 0x1c000, v209
	ds_read_b128 v[156:159], v3
	ds_read_b128 v[160:163], v3 offset:1024
	ds_read_b128 v[164:167], v3 offset:2048
	ds_read_b128 v[168:171], v3 offset:3072
	s_add_i32 s62, s62, 0x80000
	s_mov_b32 m0, s34
	ds_read_b128 v[172:175], v210 offset:32768
	ds_read_b128 v[176:179], v210 offset:33792
	ds_read_b128 v[180:183], v210 offset:34816
	ds_read_b128 v[184:187], v210 offset:35840
	ds_read_b128 v[188:191], v210 offset:36864
	ds_read_b128 v[192:195], v210 offset:37888
	ds_read_b128 v[196:199], v210 offset:38912
	ds_read_b128 v[200:203], v210 offset:39936
	buffer_load_dwordx4 v1, s[4:7], s62 offen lds
	s_mov_b32 m0, s35
	s_nop 0
	buffer_load_dwordx4 v206, s[4:7], s62 offen lds
	s_waitcnt vmcnt(8)
	s_waitcnt lgkmcnt(0)
	s_barrier
	s_setprio 1
	s_waitcnt lgkmcnt(7)
	v_mfma_f32_16x16x32_bf16 v[130:133], v[140:143], v[172:175], v[130:133]
	v_mfma_f32_16x16x32_bf16 v[126:129], v[148:151], v[172:175], v[126:129]
	s_waitcnt lgkmcnt(5)
	v_mfma_f32_16x16x32_bf16 v[122:125], v[140:143], v[180:183], v[122:125]
	v_mfma_f32_16x16x32_bf16 v[118:121], v[148:151], v[180:183], v[118:121]
	s_waitcnt lgkmcnt(3)
	v_mfma_f32_16x16x32_bf16 v[114:117], v[140:143], v[188:191], v[114:117]
	v_mfma_f32_16x16x32_bf16 v[110:113], v[148:151], v[188:191], v[110:113]
	s_waitcnt lgkmcnt(1)
	v_mfma_f32_16x16x32_bf16 v[106:109], v[140:143], v[196:199], v[106:109]
	v_mfma_f32_16x16x32_bf16 v[102:105], v[148:151], v[196:199], v[102:105]
	v_mfma_f32_16x16x32_bf16 v[130:133], v[144:147], v[176:179], v[130:133]
	v_mfma_f32_16x16x32_bf16 v[126:129], v[152:155], v[176:179], v[126:129]
	v_mfma_f32_16x16x32_bf16 v[122:125], v[144:147], v[184:187], v[122:125]
	v_mfma_f32_16x16x32_bf16 v[118:121], v[152:155], v[184:187], v[118:121]
	v_mfma_f32_16x16x32_bf16 v[114:117], v[144:147], v[192:195], v[114:117]
	v_mfma_f32_16x16x32_bf16 v[110:113], v[152:155], v[192:195], v[110:113]
	s_waitcnt lgkmcnt(0)
	v_mfma_f32_16x16x32_bf16 v[106:109], v[144:147], v[200:203], v[106:109]
	v_mfma_f32_16x16x32_bf16 v[102:105], v[152:155], v[200:203], v[102:105]
	s_setprio 0
	s_setprio 1
	v_mfma_f32_16x16x32_bf16 v[98:101], v[156:159], v[172:175], v[98:101]
	v_mfma_f32_16x16x32_bf16 v[94:97], v[164:167], v[172:175], v[94:97]
	v_mfma_f32_16x16x32_bf16 v[90:93], v[156:159], v[180:183], v[90:93]
	v_mfma_f32_16x16x32_bf16 v[86:89], v[164:167], v[180:183], v[86:89]
	v_mfma_f32_16x16x32_bf16 v[82:85], v[156:159], v[188:191], v[82:85]
	v_mfma_f32_16x16x32_bf16 v[78:81], v[164:167], v[188:191], v[78:81]
	v_mfma_f32_16x16x32_bf16 v[74:77], v[156:159], v[196:199], v[74:77]
	v_mfma_f32_16x16x32_bf16 v[70:73], v[164:167], v[196:199], v[70:73]
	v_mfma_f32_16x16x32_bf16 v[98:101], v[160:163], v[176:179], v[98:101]
	v_mfma_f32_16x16x32_bf16 v[94:97], v[168:171], v[176:179], v[94:97]
	v_mfma_f32_16x16x32_bf16 v[90:93], v[160:163], v[184:187], v[90:93]
	v_mfma_f32_16x16x32_bf16 v[86:89], v[168:171], v[184:187], v[86:89]
	v_mfma_f32_16x16x32_bf16 v[82:85], v[160:163], v[192:195], v[82:85]
	v_mfma_f32_16x16x32_bf16 v[78:81], v[168:171], v[192:195], v[78:81]
	v_mfma_f32_16x16x32_bf16 v[74:77], v[160:163], v[200:203], v[74:77]
	v_mfma_f32_16x16x32_bf16 v[70:73], v[168:171], v[200:203], v[70:73]
	s_setprio 0
	s_barrier
	s_mov_b32 m0, s38
	s_add_i32 s62, s61, 0x80
	ds_read_b128 v[172:175], v210 offset:49152
	ds_read_b128 v[176:179], v210 offset:50176
	ds_read_b128 v[180:183], v210 offset:51200
	ds_read_b128 v[184:187], v210 offset:52224
	ds_read_b128 v[188:191], v210 offset:53248
	ds_read_b128 v[192:195], v210 offset:54272
	ds_read_b128 v[196:199], v210 offset:55296
	ds_read_b128 v[200:203], v210 offset:56320
	buffer_load_dwordx4 v135, s[8:11], s62 offen lds
	s_mov_b32 m0, s39
	s_add_i32 s61, s61, 0x80080
	buffer_load_dwordx4 v207, s[8:11], s62 offen lds
	s_mov_b32 m0, s42
	s_nop 0
	buffer_load_dwordx4 v135, s[8:11], s61 offen lds
	s_mov_b32 m0, s43
	s_nop 0
	buffer_load_dwordx4 v207, s[8:11], s61 offen lds
	s_mov_b32 m0, s40
	s_nop 0
	buffer_load_dwordx4 v1, s[4:7], s60 offen lds
	s_mov_b32 m0, s41
	s_nop 0
	buffer_load_dwordx4 v206, s[4:7], s60 offen lds
	s_waitcnt vmcnt(8)
	s_waitcnt lgkmcnt(0)
	s_barrier
	s_setprio 1
	s_waitcnt lgkmcnt(7)
	v_mfma_f32_16x16x32_bf16 v[66:69], v[140:143], v[172:175], v[66:69]
	v_mfma_f32_16x16x32_bf16 v[62:65], v[148:151], v[172:175], v[62:65]
	s_waitcnt lgkmcnt(5)
	v_mfma_f32_16x16x32_bf16 v[58:61], v[140:143], v[180:183], v[58:61]
	v_mfma_f32_16x16x32_bf16 v[54:57], v[148:151], v[180:183], v[54:57]
	s_waitcnt lgkmcnt(3)
	v_mfma_f32_16x16x32_bf16 v[50:53], v[140:143], v[188:191], v[50:53]
	v_mfma_f32_16x16x32_bf16 v[46:49], v[148:151], v[188:191], v[46:49]
	s_waitcnt lgkmcnt(1)
	v_mfma_f32_16x16x32_bf16 v[42:45], v[140:143], v[196:199], v[42:45]
	v_mfma_f32_16x16x32_bf16 v[38:41], v[148:151], v[196:199], v[38:41]
	v_mfma_f32_16x16x32_bf16 v[66:69], v[144:147], v[176:179], v[66:69]
	v_mfma_f32_16x16x32_bf16 v[62:65], v[152:155], v[176:179], v[62:65]
	v_mfma_f32_16x16x32_bf16 v[58:61], v[144:147], v[184:187], v[58:61]
	v_mfma_f32_16x16x32_bf16 v[54:57], v[152:155], v[184:187], v[54:57]
	v_mfma_f32_16x16x32_bf16 v[50:53], v[144:147], v[192:195], v[50:53]
	v_mfma_f32_16x16x32_bf16 v[46:49], v[152:155], v[192:195], v[46:49]
	s_waitcnt lgkmcnt(0)
	v_mfma_f32_16x16x32_bf16 v[42:45], v[144:147], v[200:203], v[42:45]
	v_mfma_f32_16x16x32_bf16 v[38:41], v[152:155], v[200:203], v[38:41]
	s_setprio 0
	s_setprio 1
	v_mfma_f32_16x16x32_bf16 v[34:37], v[156:159], v[172:175], v[34:37]
	v_mfma_f32_16x16x32_bf16 v[30:33], v[164:167], v[172:175], v[30:33]
	v_mfma_f32_16x16x32_bf16 v[26:29], v[156:159], v[180:183], v[26:29]
	v_mfma_f32_16x16x32_bf16 v[22:25], v[164:167], v[180:183], v[22:25]
	v_mfma_f32_16x16x32_bf16 v[18:21], v[156:159], v[188:191], v[18:21]
	v_mfma_f32_16x16x32_bf16 v[14:17], v[164:167], v[188:191], v[14:17]
	v_mfma_f32_16x16x32_bf16 v[8:11], v[156:159], v[196:199], v[10:13]
	v_mfma_f32_16x16x32_bf16 v[4:7], v[164:167], v[196:199], v[4:7]
	v_mfma_f32_16x16x32_bf16 v[34:37], v[160:163], v[176:179], v[34:37]
	v_mfma_f32_16x16x32_bf16 v[30:33], v[168:171], v[176:179], v[30:33]
	v_mfma_f32_16x16x32_bf16 v[26:29], v[160:163], v[184:187], v[26:29]
	v_mfma_f32_16x16x32_bf16 v[22:25], v[168:171], v[184:187], v[22:25]
	v_mfma_f32_16x16x32_bf16 v[18:21], v[160:163], v[192:195], v[18:21]
	v_mfma_f32_16x16x32_bf16 v[14:17], v[168:171], v[192:195], v[14:17]
	v_mfma_f32_16x16x32_bf16 v[10:13], v[160:163], v[200:203], v[8:11]
	v_mfma_f32_16x16x32_bf16 v[6:9], v[168:171], v[200:203], v[4:7]
	s_setprio 0
	s_barrier
	s_add_i32 s59, s59, 2
	s_addk_i32 s57, 0x100
	s_addk_i32 s58, 0x100
	s_cmp_gt_u32 s59, 13
	s_cbranch_scc0 .LBB0_563
	s_and_b64 vcc, exec, s[20:21]
	s_cbranch_vccz .LBB0_566
	s_barrier
.LBB0_566:
	s_lshl_b32 s2, s22, 8
	v_lshl_add_u32 v4, s23, 8, v208
	s_ashr_i32 s3, s2, 31
	v_ashrrev_i32_e32 v5, 31, v4
	s_cmp_lg_u32 s56, 0
	v_lshlrev_b64 v[4:5], 11, v[4:5]
	s_cselect_b64 s[10:11], -1, 0
	s_cmp_eq_u32 s56, 0
	v_lshl_add_u64 v[4:5], v[4:5], 0, s[2:3]
	s_cselect_b64 s[2:3], -1, 0
	s_and_b64 s[2:3], s[2:3], exec
	v_readlane_b32 s56, v255, 1
	s_cselect_b32 s22, s46, 0x11b00000
	v_readlane_b32 s58, v255, 3
	v_readlane_b32 s59, v255, 4
	s_add_u32 s22, s58, s22
	v_or_b32_e32 v4, v4, v134
	s_addc_u32 s23, s59, 0
	v_lshl_add_u64 v[140:141], v[4:5], 1, s[22:23]
	v_add_co_u32_e32 v154, vcc, 0x10000, v140
	global_load_dwordx4 v[142:145], v[140:141], off nt
	global_load_dwordx4 v[146:149], v[140:141], off offset:256 nt
	v_addc_co_u32_e32 v155, vcc, 0, v141, vcc
	v_add_co_u32_e32 v162, vcc, 0x20000, v140
	global_load_dwordx4 v[150:153], v[154:155], off nt
	s_nop 0
	global_load_dwordx4 v[154:157], v[154:155], off offset:256 nt
	v_addc_co_u32_e32 v163, vcc, 0, v141, vcc
	global_load_dwordx4 v[158:161], v[162:163], off nt
	v_add_co_u32_e32 v162, vcc, 0x30000, v140
	s_mov_b64 s[22:23], -1
	s_nop 0
	v_addc_co_u32_e32 v163, vcc, 0, v141, vcc
	v_add_co_u32_e32 v252, vcc, s37, v140
	s_nop 1
	v_addc_co_u32_e32 v253, vcc, 0, v141, vcc
	v_add_co_u32_e32 v252, vcc, s48, v140
	s_nop 1
	v_addc_co_u32_e32 v253, vcc, 0, v141, vcc
	v_add_co_u32_e32 v252, vcc, 0xa0000, v140
	s_nop 1
	v_addc_co_u32_e32 v253, vcc, 0, v141, vcc
	v_add_co_u32_e32 v252, vcc, 0xb0000, v140
	s_nop 1
	v_addc_co_u32_e32 v253, vcc, 0, v141, vcc
	v_lshl_add_u64 v[4:5], v[4:5], 1, s[18:19]
	s_mov_b64 vcc, s[2:3]
	v_readlane_b32 s57, v255, 2
	v_readlane_b32 s60, v255, 5
	v_readlane_b32 s61, v255, 6
	v_readlane_b32 s62, v255, 7
	v_readlane_b32 s63, v255, 8
	s_waitcnt vmcnt(4)
	v_cvt_f32_f16_sdwa v203, v142 dst_sel:DWORD dst_unused:UNUSED_PAD src0_sel:WORD_1
	v_cvt_f32_f16_e32 v202, v142
	v_cvt_f32_f16_sdwa v205, v143 dst_sel:DWORD dst_unused:UNUSED_PAD src0_sel:WORD_1
	v_cvt_f32_f16_e32 v204, v143
	v_cvt_f32_f16_sdwa v199, v144 dst_sel:DWORD dst_unused:UNUSED_PAD src0_sel:WORD_1
	v_cvt_f32_f16_e32 v198, v144
	v_cvt_f32_f16_sdwa v201, v145 dst_sel:DWORD dst_unused:UNUSED_PAD src0_sel:WORD_1
	v_cvt_f32_f16_e32 v200, v145
	s_waitcnt vmcnt(3)
	v_cvt_f32_f16_sdwa v195, v146 dst_sel:DWORD dst_unused:UNUSED_PAD src0_sel:WORD_1
	v_cvt_f32_f16_e32 v194, v146
	v_cvt_f32_f16_sdwa v197, v147 dst_sel:DWORD dst_unused:UNUSED_PAD src0_sel:WORD_1
	v_cvt_f32_f16_e32 v196, v147
	v_cvt_f32_f16_sdwa v191, v148 dst_sel:DWORD dst_unused:UNUSED_PAD src0_sel:WORD_1
	v_cvt_f32_f16_e32 v190, v148
	v_cvt_f32_f16_sdwa v193, v149 dst_sel:DWORD dst_unused:UNUSED_PAD src0_sel:WORD_1
	v_cvt_f32_f16_e32 v192, v149
	s_waitcnt vmcnt(2)
	v_cvt_f32_f16_sdwa v187, v150 dst_sel:DWORD dst_unused:UNUSED_PAD src0_sel:WORD_1
	v_cvt_f32_f16_e32 v186, v150
	v_cvt_f32_f16_sdwa v189, v151 dst_sel:DWORD dst_unused:UNUSED_PAD src0_sel:WORD_1
	v_cvt_f32_f16_e32 v188, v151
	v_cvt_f32_f16_sdwa v183, v152 dst_sel:DWORD dst_unused:UNUSED_PAD src0_sel:WORD_1
	v_cvt_f32_f16_e32 v182, v152
	v_cvt_f32_f16_sdwa v185, v153 dst_sel:DWORD dst_unused:UNUSED_PAD src0_sel:WORD_1
	v_cvt_f32_f16_e32 v184, v153
	s_waitcnt vmcnt(1)
	v_cvt_f32_f16_sdwa v179, v154 dst_sel:DWORD dst_unused:UNUSED_PAD src0_sel:WORD_1
	v_cvt_f32_f16_e32 v178, v154
	v_cvt_f32_f16_sdwa v181, v155 dst_sel:DWORD dst_unused:UNUSED_PAD src0_sel:WORD_1
	v_cvt_f32_f16_e32 v180, v155
	v_cvt_f32_f16_sdwa v175, v156 dst_sel:DWORD dst_unused:UNUSED_PAD src0_sel:WORD_1
	v_cvt_f32_f16_e32 v174, v156
	v_cvt_f32_f16_sdwa v177, v157 dst_sel:DWORD dst_unused:UNUSED_PAD src0_sel:WORD_1
	v_cvt_f32_f16_e32 v176, v157
	s_waitcnt vmcnt(0)
	v_cvt_f32_f16_sdwa v171, v158 dst_sel:DWORD dst_unused:UNUSED_PAD src0_sel:WORD_1
	v_cvt_f32_f16_e32 v170, v158
	v_cvt_f32_f16_sdwa v173, v159 dst_sel:DWORD dst_unused:UNUSED_PAD src0_sel:WORD_1
	v_cvt_f32_f16_e32 v172, v159
	v_cvt_f32_f16_sdwa v167, v160 dst_sel:DWORD dst_unused:UNUSED_PAD src0_sel:WORD_1
	v_cvt_f32_f16_e32 v166, v160
	v_cvt_f32_f16_sdwa v169, v161 dst_sel:DWORD dst_unused:UNUSED_PAD src0_sel:WORD_1
	v_cvt_f32_f16_e32 v168, v161
	s_waitcnt vmcnt(0)
	v_cvt_f32_f16_sdwa v163, v212 dst_sel:DWORD dst_unused:UNUSED_PAD src0_sel:WORD_1
	v_cvt_f32_f16_e32 v162, v212
	v_cvt_f32_f16_sdwa v165, v213 dst_sel:DWORD dst_unused:UNUSED_PAD src0_sel:WORD_1
	v_cvt_f32_f16_e32 v164, v213
	v_cvt_f32_f16_sdwa v159, v214 dst_sel:DWORD dst_unused:UNUSED_PAD src0_sel:WORD_1
	v_cvt_f32_f16_e32 v158, v214
	v_cvt_f32_f16_sdwa v161, v215 dst_sel:DWORD dst_unused:UNUSED_PAD src0_sel:WORD_1
	v_cvt_f32_f16_e32 v160, v215
	s_waitcnt vmcnt(0)
	v_cvt_f32_f16_sdwa v155, v216 dst_sel:DWORD dst_unused:UNUSED_PAD src0_sel:WORD_1
	v_cvt_f32_f16_e32 v154, v216
	v_cvt_f32_f16_sdwa v157, v217 dst_sel:DWORD dst_unused:UNUSED_PAD src0_sel:WORD_1
	v_cvt_f32_f16_e32 v156, v217
	v_cvt_f32_f16_sdwa v151, v218 dst_sel:DWORD dst_unused:UNUSED_PAD src0_sel:WORD_1
	v_cvt_f32_f16_e32 v150, v218
	v_cvt_f32_f16_sdwa v153, v219 dst_sel:DWORD dst_unused:UNUSED_PAD src0_sel:WORD_1
	v_cvt_f32_f16_e32 v152, v219
	s_waitcnt vmcnt(0)
	v_cvt_f32_f16_sdwa v147, v220 dst_sel:DWORD dst_unused:UNUSED_PAD src0_sel:WORD_1
	v_cvt_f32_f16_e32 v146, v220
	v_cvt_f32_f16_sdwa v149, v221 dst_sel:DWORD dst_unused:UNUSED_PAD src0_sel:WORD_1
	v_cvt_f32_f16_e32 v148, v221
	v_cvt_f32_f16_sdwa v143, v222 dst_sel:DWORD dst_unused:UNUSED_PAD src0_sel:WORD_1
	v_cvt_f32_f16_e32 v142, v222
	v_cvt_f32_f16_sdwa v145, v223 dst_sel:DWORD dst_unused:UNUSED_PAD src0_sel:WORD_1
	v_cvt_f32_f16_e32 v144, v223
	global_load_dwordx2 v[222:223], v[252:253], off offset:264 nt
	global_load_dwordx2 v[252:253], v[252:253], off offset:256 nt
	s_cbranch_vccnz .LBB0_568
	v_pk_mul_f32 v[212:213], v[130:131], v[202:203]
	v_pk_mul_f32 v[214:215], v[132:133], v[204:205]
	v_pk_mul_f32 v[216:217], v[126:127], v[198:199]
	v_pk_mul_f32 v[218:219], v[128:129], v[200:201]
	v_cvt_pk_bf16_f32 v212, v212, v213
	v_cvt_pk_bf16_f32 v213, v214, v215
	v_cvt_pk_bf16_f32 v214, v216, v217
	v_cvt_pk_bf16_f32 v215, v218, v219
	global_store_dwordx4 v[4:5], v[212:215], off
	v_pk_mul_f32 v[216:217], v[94:95], v[190:191]
	v_pk_mul_f32 v[218:219], v[96:97], v[192:193]
	v_pk_mul_f32 v[212:213], v[98:99], v[194:195]
	v_pk_mul_f32 v[214:215], v[100:101], v[196:197]
	v_cvt_pk_bf16_f32 v212, v212, v213
	v_cvt_pk_bf16_f32 v213, v214, v215
	v_cvt_pk_bf16_f32 v214, v216, v217
	v_cvt_pk_bf16_f32 v215, v218, v219
	global_store_dwordx4 v[4:5], v[212:215], off offset:256
	v_pk_mul_f32 v[216:217], v[118:119], v[182:183]
	v_pk_mul_f32 v[218:219], v[120:121], v[184:185]
	v_pk_mul_f32 v[212:213], v[122:123], v[186:187]
	v_pk_mul_f32 v[214:215], v[124:125], v[188:189]
	v_cvt_pk_bf16_f32 v212, v212, v213
	v_cvt_pk_bf16_f32 v213, v214, v215
	v_cvt_pk_bf16_f32 v214, v216, v217
	v_add_co_u32_e32 v216, vcc, s36, v4
	v_cvt_pk_bf16_f32 v215, v218, v219
	s_nop 0
	v_addc_co_u32_e32 v217, vcc, 0, v5, vcc
	global_store_dwordx4 v[216:217], v[212:215], off
	v_pk_mul_f32 v[218:219], v[86:87], v[174:175]
	v_pk_mul_f32 v[220:221], v[88:89], v[176:177]
	v_pk_mul_f32 v[212:213], v[90:91], v[178:179]
	v_pk_mul_f32 v[214:215], v[92:93], v[180:181]
	v_cvt_pk_bf16_f32 v212, v212, v213
	v_cvt_pk_bf16_f32 v213, v214, v215
	v_cvt_pk_bf16_f32 v214, v218, v219
	v_cvt_pk_bf16_f32 v215, v220, v221
	global_store_dwordx4 v[216:217], v[212:215], off offset:256
	v_pk_mul_f32 v[216:217], v[110:111], v[166:167]
	v_pk_mul_f32 v[218:219], v[112:113], v[168:169]
	v_pk_mul_f32 v[212:213], v[114:115], v[170:171]
	v_pk_mul_f32 v[214:215], v[116:117], v[172:173]
	v_cvt_pk_bf16_f32 v212, v212, v213
	v_cvt_pk_bf16_f32 v213, v214, v215
	v_cvt_pk_bf16_f32 v214, v216, v217
	v_add_co_u32_e32 v216, vcc, s7, v4
	v_cvt_pk_bf16_f32 v215, v218, v219
	s_nop 0
	v_addc_co_u32_e32 v217, vcc, 0, v5, vcc
	global_store_dwordx4 v[216:217], v[212:215], off
	v_pk_mul_f32 v[218:219], v[78:79], v[158:159]
	v_pk_mul_f32 v[220:221], v[80:81], v[160:161]
	v_pk_mul_f32 v[212:213], v[82:83], v[162:163]
	v_pk_mul_f32 v[214:215], v[84:85], v[164:165]
	v_cvt_pk_bf16_f32 v212, v212, v213
	v_cvt_pk_bf16_f32 v213, v214, v215
	v_cvt_pk_bf16_f32 v214, v218, v219
	v_cvt_pk_bf16_f32 v215, v220, v221
	global_store_dwordx4 v[216:217], v[212:215], off offset:256
	v_pk_mul_f32 v[216:217], v[102:103], v[150:151]
	v_pk_mul_f32 v[218:219], v[104:105], v[152:153]
	v_pk_mul_f32 v[212:213], v[106:107], v[154:155]
	v_pk_mul_f32 v[214:215], v[108:109], v[156:157]
	v_cvt_pk_bf16_f32 v212, v212, v213
	v_cvt_pk_bf16_f32 v213, v214, v215
	v_cvt_pk_bf16_f32 v214, v216, v217
	v_add_co_u32_e32 v216, vcc, s47, v4
	v_cvt_pk_bf16_f32 v215, v218, v219
	s_nop 0
	v_addc_co_u32_e32 v217, vcc, 0, v5, vcc
	global_store_dwordx4 v[216:217], v[212:215], off
	v_pk_mul_f32 v[218:219], v[70:71], v[142:143]
	v_pk_mul_f32 v[220:221], v[72:73], v[144:145]
	v_pk_mul_f32 v[212:213], v[74:75], v[146:147]
	v_pk_mul_f32 v[214:215], v[76:77], v[148:149]
	v_cvt_pk_bf16_f32 v212, v212, v213
	v_cvt_pk_bf16_f32 v213, v214, v215
	v_cvt_pk_bf16_f32 v214, v218, v219
	v_cvt_pk_bf16_f32 v215, v220, v221
	s_mov_b64 s[22:23], 0
	global_store_dwordx4 v[216:217], v[212:215], off offset:256

.LBB0_729:
	s_or_b64 exec, exec, s[6:7]
	s_waitcnt lgkmcnt(0)
	s_barrier
	v_lshl_add_u32 v222, v226, 2, 0
	ds_read_b32 v230, v222 offset:8192
	v_readlane_b32 s36, v255, 21
	v_readlane_b32 s37, v255, 22
	s_mov_b64 s[4:5], s[36:37]
	v_readlane_b32 s38, v255, 23
	s_waitcnt lgkmcnt(0)
	v_pk_mul_f32 v[126:127], v[126:127], v[230:231] op_sel_hi:[1,0]
	v_pk_mul_f32 v[128:129], v[128:129], v[230:231] op_sel_hi:[1,0]
	v_pk_mul_f32 v[122:123], v[122:123], v[230:231] op_sel_hi:[1,0]
	v_pk_mul_f32 v[124:125], v[124:125], v[230:231] op_sel_hi:[1,0]
	v_pk_mul_f32 v[118:119], v[118:119], v[230:231] op_sel_hi:[1,0]
	v_pk_mul_f32 v[120:121], v[120:121], v[230:231] op_sel_hi:[1,0]
	v_pk_mul_f32 v[114:115], v[114:115], v[230:231] op_sel_hi:[1,0]
	v_pk_mul_f32 v[116:117], v[116:117], v[230:231] op_sel_hi:[1,0]
	s_waitcnt vmcnt(2)
	v_pk_fma_f32 v[128:129], v[144:145], v[128:129], v[208:209]
	v_pk_fma_f32 v[126:127], v[142:143], v[126:127], v[206:207]
	v_pk_fma_f32 v[124:125], v[136:137], v[124:125], v[204:205]
	v_pk_fma_f32 v[122:123], v[134:135], v[122:123], v[202:203]
	s_waitcnt vmcnt(0)
	v_pk_fma_f32 v[120:121], v[140:141], v[120:121], v[200:201]
	v_pk_fma_f32 v[118:119], v[138:139], v[118:119], v[198:199]
	v_pk_fma_f32 v[116:117], v[132:133], v[116:117], v[196:197]
	v_pk_fma_f32 v[114:115], v[130:131], v[114:115], v[194:195]
	v_readlane_b32 s39, v255, 24
	ds_read_b32 v194, v222 offset:8256
	v_readlane_b32 s40, v255, 25
	v_readlane_b32 s41, v255, 26
	v_readlane_b32 s42, v255, 27
	v_readlane_b32 s43, v255, 28
	s_waitcnt lgkmcnt(0)
	v_pk_mul_f32 v[110:111], v[110:111], v[194:195] op_sel_hi:[1,0]
	v_pk_mul_f32 v[112:113], v[112:113], v[194:195] op_sel_hi:[1,0]
	v_pk_mul_f32 v[106:107], v[106:107], v[194:195] op_sel_hi:[1,0]
	v_pk_mul_f32 v[108:109], v[108:109], v[194:195] op_sel_hi:[1,0]
	v_pk_mul_f32 v[102:103], v[102:103], v[194:195] op_sel_hi:[1,0]
	v_pk_mul_f32 v[104:105], v[104:105], v[194:195] op_sel_hi:[1,0]
	v_pk_mul_f32 v[94:95], v[94:95], v[194:195] op_sel_hi:[1,0]
	v_pk_mul_f32 v[96:97], v[96:97], v[194:195] op_sel_hi:[1,0]
	v_pk_fma_f32 v[112:113], v[144:145], v[112:113], v[192:193]
	v_pk_fma_f32 v[110:111], v[142:143], v[110:111], v[190:191]
	v_pk_fma_f32 v[108:109], v[136:137], v[108:109], v[188:189]
	v_pk_fma_f32 v[106:107], v[134:135], v[106:107], v[186:187]
	v_pk_fma_f32 v[104:105], v[140:141], v[104:105], v[184:185]
	v_pk_fma_f32 v[102:103], v[138:139], v[102:103], v[182:183]
	v_pk_fma_f32 v[96:97], v[132:133], v[96:97], v[180:181]
	v_pk_fma_f32 v[94:95], v[130:131], v[94:95], v[178:179]
	v_readlane_b32 s44, v255, 29
	ds_read_b32 v178, v222 offset:8320
	v_readlane_b32 s45, v255, 30
	v_readlane_b32 s46, v255, 31
	v_readlane_b32 s47, v255, 32
	v_readlane_b32 s48, v255, 33
	s_waitcnt lgkmcnt(0)
	v_pk_mul_f32 v[98:99], v[98:99], v[178:179] op_sel_hi:[1,0]
	v_pk_mul_f32 v[100:101], v[100:101], v[178:179] op_sel_hi:[1,0]
	v_pk_mul_f32 v[90:91], v[90:91], v[178:179] op_sel_hi:[1,0]
	v_pk_mul_f32 v[92:93], v[92:93], v[178:179] op_sel_hi:[1,0]
	v_pk_mul_f32 v[86:87], v[86:87], v[178:179] op_sel_hi:[1,0]
	v_pk_mul_f32 v[88:89], v[88:89], v[178:179] op_sel_hi:[1,0]
	v_pk_mul_f32 v[78:79], v[78:79], v[178:179] op_sel_hi:[1,0]
	v_pk_mul_f32 v[80:81], v[80:81], v[178:179] op_sel_hi:[1,0]
	v_pk_fma_f32 v[100:101], v[144:145], v[100:101], v[176:177]
	v_pk_fma_f32 v[98:99], v[142:143], v[98:99], v[174:175]
	v_pk_fma_f32 v[92:93], v[136:137], v[92:93], v[172:173]
	v_pk_fma_f32 v[90:91], v[134:135], v[90:91], v[170:171]
	v_pk_fma_f32 v[88:89], v[140:141], v[88:89], v[168:169]
	v_pk_fma_f32 v[86:87], v[138:139], v[86:87], v[166:167]
	v_pk_fma_f32 v[80:81], v[132:133], v[80:81], v[164:165]
	v_pk_fma_f32 v[78:79], v[130:131], v[78:79], v[162:163]
	v_add_u32_e32 v172, s22, v226
	ds_read_b32 v162, v222 offset:8384
	v_readlane_b32 s49, v255, 34
	v_readlane_b32 s50, v255, 35
	v_readlane_b32 s51, v255, 36
	s_waitcnt lgkmcnt(0)
	v_pk_mul_f32 v[66:67], v[66:67], v[162:163] op_sel_hi:[1,0]
	s_nop 0
	v_pk_fma_f32 v[66:67], v[130:131], v[66:67], v[146:147]
	v_add_u32_e32 v146, 0x80, v172
	v_ashrrev_i32_e32 v147, 31, v146
	v_lshlrev_b64 v[146:147], 13, v[146:147]
	v_pk_mul_f32 v[82:83], v[82:83], v[162:163] op_sel_hi:[1,0]
	v_pk_mul_f32 v[84:85], v[84:85], v[162:163] op_sel_hi:[1,0]
	v_pk_mul_f32 v[74:75], v[74:75], v[162:163] op_sel_hi:[1,0]
	v_pk_mul_f32 v[76:77], v[76:77], v[162:163] op_sel_hi:[1,0]
	v_pk_mul_f32 v[70:71], v[70:71], v[162:163] op_sel_hi:[1,0]
	v_pk_mul_f32 v[72:73], v[72:73], v[162:163] op_sel_hi:[1,0]
	v_pk_mul_f32 v[68:69], v[68:69], v[162:163] op_sel_hi:[1,0]
	v_lshl_add_u64 v[146:147], s[4:5], 0, v[146:147]
	v_pk_fma_f32 v[84:85], v[144:145], v[84:85], v[160:161]
	v_pk_fma_f32 v[82:83], v[142:143], v[82:83], v[158:159]
	v_pk_fma_f32 v[76:77], v[136:137], v[76:77], v[156:157]
	v_pk_fma_f32 v[74:75], v[134:135], v[74:75], v[154:155]
	v_pk_fma_f32 v[72:73], v[140:141], v[72:73], v[152:153]
	v_pk_fma_f32 v[70:71], v[138:139], v[70:71], v[150:151]
	v_pk_fma_f32 v[68:69], v[132:133], v[68:69], v[148:149]
	v_lshl_add_u64 v[158:159], v[146:147], 0, v[220:221]
	global_load_dwordx4 v[146:149], v[158:159], off
	global_load_dwordx4 v[150:153], v[158:159], off offset:16
	global_load_dwordx4 v[154:157], v[158:159], off offset:512
	s_nop 0
	global_load_dwordx4 v[158:161], v[158:159], off offset:528
	ds_read_b32 v164, v222 offset:8704
	v_add_u32_e32 v162, 0x90, v172
	v_ashrrev_i32_e32 v163, 31, v162
	v_lshlrev_b64 v[162:163], 13, v[162:163]
	v_lshl_add_u64 v[162:163], s[4:5], 0, v[162:163]
	s_waitcnt lgkmcnt(0)
	v_pk_mul_f32 v[62:63], v[62:63], v[164:165] op_sel_hi:[1,0]
	v_pk_mul_f32 v[64:65], v[64:65], v[164:165] op_sel_hi:[1,0]
	v_pk_mul_f32 v[166:167], v[58:59], v[164:165] op_sel_hi:[1,0]
	v_pk_mul_f32 v[168:169], v[60:61], v[164:165] op_sel_hi:[1,0]
	v_pk_mul_f32 v[54:55], v[54:55], v[164:165] op_sel_hi:[1,0]
	v_pk_mul_f32 v[56:57], v[56:57], v[164:165] op_sel_hi:[1,0]
	v_pk_mul_f32 v[170:171], v[50:51], v[164:165] op_sel_hi:[1,0]
	v_pk_mul_f32 v[164:165], v[52:53], v[164:165] op_sel_hi:[1,0]
	v_lshl_add_u64 v[162:163], v[162:163], 0, v[220:221]
	s_waitcnt vmcnt(3)
	v_pk_fma_f32 v[60:61], v[144:145], v[64:65], v[148:149]
	v_pk_fma_f32 v[58:59], v[142:143], v[62:63], v[146:147]
	s_waitcnt vmcnt(2)
	v_pk_fma_f32 v[64:65], v[136:137], v[168:169], v[152:153]
	v_pk_fma_f32 v[62:63], v[134:135], v[166:167], v[150:151]
	s_waitcnt vmcnt(1)
	v_pk_fma_f32 v[52:53], v[140:141], v[56:57], v[156:157]
	v_pk_fma_f32 v[50:51], v[138:139], v[54:55], v[154:155]
	s_waitcnt vmcnt(0)
	v_pk_fma_f32 v[56:57], v[132:133], v[164:165], v[160:161]
	v_pk_fma_f32 v[54:55], v[130:131], v[170:171], v[158:159]
	s_nop 0
	global_load_dwordx4 v[146:149], v[162:163], off
	global_load_dwordx4 v[150:153], v[162:163], off offset:16
	global_load_dwordx4 v[154:157], v[162:163], off offset:512
	global_load_dwordx4 v[158:161], v[162:163], off offset:528
	ds_read_b32 v164, v222 offset:8768
	v_add_u32_e32 v162, 0xa0, v172
	v_ashrrev_i32_e32 v163, 31, v162
	v_lshlrev_b64 v[162:163], 13, v[162:163]
	v_lshl_add_u64 v[162:163], s[4:5], 0, v[162:163]
	s_waitcnt lgkmcnt(0)
	v_pk_mul_f32 v[46:47], v[46:47], v[164:165] op_sel_hi:[1,0]
	v_pk_mul_f32 v[48:49], v[48:49], v[164:165] op_sel_hi:[1,0]
	v_pk_mul_f32 v[166:167], v[42:43], v[164:165] op_sel_hi:[1,0]
	v_pk_mul_f32 v[168:169], v[44:45], v[164:165] op_sel_hi:[1,0]
	v_pk_mul_f32 v[38:39], v[38:39], v[164:165] op_sel_hi:[1,0]
	v_pk_mul_f32 v[40:41], v[40:41], v[164:165] op_sel_hi:[1,0]
	v_pk_mul_f32 v[170:171], v[34:35], v[164:165] op_sel_hi:[1,0]
	v_pk_mul_f32 v[164:165], v[36:37], v[164:165] op_sel_hi:[1,0]
	v_lshl_add_u64 v[162:163], v[162:163], 0, v[220:221]
	s_waitcnt vmcnt(3)
	v_pk_fma_f32 v[44:45], v[144:145], v[48:49], v[148:149]
	v_pk_fma_f32 v[42:43], v[142:143], v[46:47], v[146:147]
	s_waitcnt vmcnt(2)
	v_pk_fma_f32 v[48:49], v[136:137], v[168:169], v[152:153]
	v_pk_fma_f32 v[46:47], v[134:135], v[166:167], v[150:151]
	s_waitcnt vmcnt(1)
	v_pk_fma_f32 v[36:37], v[140:141], v[40:41], v[156:157]
	v_pk_fma_f32 v[34:35], v[138:139], v[38:39], v[154:155]
	s_waitcnt vmcnt(0)
	v_pk_fma_f32 v[40:41], v[132:133], v[164:165], v[160:161]
	v_pk_fma_f32 v[38:39], v[130:131], v[170:171], v[158:159]
	s_nop 0
	global_load_dwordx4 v[146:149], v[162:163], off
	global_load_dwordx4 v[150:153], v[162:163], off offset:16
	global_load_dwordx4 v[154:157], v[162:163], off offset:512
	global_load_dwordx4 v[158:161], v[162:163], off offset:528
	ds_read_b32 v164, v222 offset:8832
	v_add_u32_e32 v162, 0xb0, v172
	v_ashrrev_i32_e32 v163, 31, v162
	v_lshlrev_b64 v[162:163], 13, v[162:163]
	v_lshl_add_u64 v[162:163], s[4:5], 0, v[162:163]
	s_waitcnt lgkmcnt(0)
	v_pk_mul_f32 v[30:31], v[30:31], v[164:165] op_sel_hi:[1,0]
	v_pk_mul_f32 v[32:33], v[32:33], v[164:165] op_sel_hi:[1,0]
	v_pk_mul_f32 v[166:167], v[26:27], v[164:165] op_sel_hi:[1,0]
	v_pk_mul_f32 v[168:169], v[28:29], v[164:165] op_sel_hi:[1,0]
	v_pk_mul_f32 v[22:23], v[22:23], v[164:165] op_sel_hi:[1,0]
	v_pk_mul_f32 v[24:25], v[24:25], v[164:165] op_sel_hi:[1,0]
	v_pk_mul_f32 v[170:171], v[18:19], v[164:165] op_sel_hi:[1,0]
	v_pk_mul_f32 v[164:165], v[20:21], v[164:165] op_sel_hi:[1,0]
	v_lshl_add_u64 v[162:163], v[162:163], 0, v[220:221]
	s_waitcnt vmcnt(3)
	v_pk_fma_f32 v[28:29], v[144:145], v[32:33], v[148:149]
	v_pk_fma_f32 v[26:27], v[142:143], v[30:31], v[146:147]
	s_waitcnt vmcnt(2)
	v_pk_fma_f32 v[32:33], v[136:137], v[168:169], v[152:153]
	v_pk_fma_f32 v[30:31], v[134:135], v[166:167], v[150:151]
	s_waitcnt vmcnt(1)
	v_pk_fma_f32 v[20:21], v[140:141], v[24:25], v[156:157]
	v_pk_fma_f32 v[18:19], v[138:139], v[22:23], v[154:155]
	s_waitcnt vmcnt(0)
	v_pk_fma_f32 v[24:25], v[132:133], v[164:165], v[160:161]
	v_pk_fma_f32 v[22:23], v[130:131], v[170:171], v[158:159]
	v_mul_f32_e32 v146, v127, v127
	global_load_dwordx4 v[148:151], v[162:163], off
	global_load_dwordx4 v[152:155], v[162:163], off offset:16
	global_load_dwordx4 v[156:159], v[162:163], off offset:512
	s_nop 0
	global_load_dwordx4 v[160:163], v[162:163], off offset:528
	v_mul_f32_e32 v147, v129, v129
	v_mul_f32_e32 v164, v123, v123
	v_mul_f32_e32 v165, v125, v125
	v_mul_f32_e32 v166, v119, v119
	v_mul_f32_e32 v167, v121, v121
	v_fmac_f32_e32 v146, v126, v126
	v_fmac_f32_e32 v147, v128, v128
	v_fmac_f32_e32 v164, v122, v122
	v_fmac_f32_e32 v165, v124, v124
	v_mul_f32_e32 v168, v115, v115
	v_mul_f32_e32 v169, v117, v117
	v_fmac_f32_e32 v166, v118, v118
	v_fmac_f32_e32 v167, v120, v120
	v_add_f32_e32 v146, v146, v147
	v_add_f32_e32 v147, v164, v165
	v_fmac_f32_e32 v168, v114, v114
	v_fmac_f32_e32 v169, v116, v116
	v_add_f32_e32 v164, v166, v167
	v_add_f32_e32 v146, v146, v147
	v_add_f32_e32 v165, v168, v169
	v_add_f32_e32 v146, v164, v146
	v_add_f32_e32 v146, v165, v146
	ds_bpermute_b32 v147, v227, v146
	ds_read_b32 v164, v222 offset:8896
	s_waitcnt lgkmcnt(1)
	v_add_f32_e32 v146, v146, v147
	ds_bpermute_b32 v147, v229, v146
	s_waitcnt lgkmcnt(1)
	v_pk_mul_f32 v[14:15], v[14:15], v[164:165] op_sel_hi:[1,0]
	v_pk_mul_f32 v[16:17], v[16:17], v[164:165] op_sel_hi:[1,0]
	v_pk_mul_f32 v[166:167], v[10:11], v[164:165] op_sel_hi:[1,0]
	v_pk_mul_f32 v[168:169], v[12:13], v[164:165] op_sel_hi:[1,0]
	v_pk_mul_f32 v[6:7], v[6:7], v[164:165] op_sel_hi:[1,0]
	v_pk_mul_f32 v[8:9], v[8:9], v[164:165] op_sel_hi:[1,0]
	v_pk_mul_f32 v[170:171], v[2:3], v[164:165] op_sel_hi:[1,0]
	v_pk_mul_f32 v[164:165], v[4:5], v[164:165] op_sel_hi:[1,0]
	s_waitcnt vmcnt(3)
	v_pk_fma_f32 v[12:13], v[144:145], v[16:17], v[150:151]
	v_pk_fma_f32 v[10:11], v[142:143], v[14:15], v[148:149]
	s_waitcnt vmcnt(2)
	v_pk_fma_f32 v[16:17], v[136:137], v[168:169], v[154:155]
	v_pk_fma_f32 v[14:15], v[134:135], v[166:167], v[152:153]
	s_waitcnt vmcnt(1)
	v_pk_fma_f32 v[4:5], v[140:141], v[8:9], v[158:159]
	v_pk_fma_f32 v[2:3], v[138:139], v[6:7], v[156:157]
	s_waitcnt vmcnt(0)
	v_pk_fma_f32 v[8:9], v[132:133], v[164:165], v[162:163]
	v_pk_fma_f32 v[6:7], v[130:131], v[170:171], v[160:161]
	s_nop 0
	s_and_saveexec_b64 s[4:5], s[0:1]
	s_cbranch_execz .LBB0_731
	s_lshl_b32 s6, s18, 10
	s_add_i32 s6, s21, s6
	v_lshl_add_u32 v130, v1, 4, s6
	s_waitcnt lgkmcnt(0)
	v_add_f32_e32 v131, v146, v147
	ds_write_b32 v130, v131

	.amdhsa_kernel _Z10hybrid_fwd4Args
		.amdhsa_group_segment_fixed_size 0
		.amdhsa_private_segment_fixed_size 0
		.amdhsa_kernarg_size 128
		.amdhsa_user_sgpr_count 2
		.amdhsa_user_sgpr_dispatch_ptr 0
		.amdhsa_user_sgpr_queue_ptr 0
		.amdhsa_user_sgpr_kernarg_segment_ptr 1
		.amdhsa_user_sgpr_dispatch_id 0
		.amdhsa_user_sgpr_kernarg_preload_length 0
		.amdhsa_user_sgpr_kernarg_preload_offset 0
		.amdhsa_user_sgpr_private_segment_size 0
		.amdhsa_uses_dynamic_stack 0
		.amdhsa_enable_private_segment 0
		.amdhsa_system_sgpr_workgroup_id_x 1
		.amdhsa_system_sgpr_workgroup_id_y 0
		.amdhsa_system_sgpr_workgroup_id_z 0
		.amdhsa_system_sgpr_workgroup_info 0
		.amdhsa_system_vgpr_workitem_id 0
		.amdhsa_next_free_vgpr 256
		.amdhsa_next_free_sgpr 102
		.amdhsa_accum_offset 256
		.amdhsa_reserve_vcc 1
		.amdhsa_float_round_mode_32 0
		.amdhsa_float_round_mode_16_64 0
		.amdhsa_float_denorm_mode_32 3
		.amdhsa_float_denorm_mode_16_64 3
		.amdhsa_dx10_clamp 1
		.amdhsa_ieee_mode 1
		.amdhsa_fp16_overflow 0
		.amdhsa_tg_split 0
		.amdhsa_exception_fp_ieee_invalid_op 0
		.amdhsa_exception_fp_denorm_src 0
		.amdhsa_exception_fp_ieee_div_zero 0
		.amdhsa_exception_fp_ieee_overflow 0
		.amdhsa_exception_fp_ieee_underflow 0
		.amdhsa_exception_fp_ieee_inexact 0
		.amdhsa_exception_int_div_zero 0
	.end_amdhsa_kernel

amdhsa.kernels:
  - .agpr_count:     0
    .args:
      - .offset:         0
        .size:           128
        .value_kind:     by_value
    .group_segment_fixed_size: 0
    .kernarg_segment_align: 8
    .kernarg_segment_size: 128
    .language:       OpenCL C
    .language_version:
      - 2
      - 0
    .max_flat_workgroup_size: 512
    .name:           _Z10hybrid_fwd4Args
    .private_segment_fixed_size: 0
    .sgpr_count:     108
    .sgpr_spill_count: 77
    .symbol:         _Z10hybrid_fwd4Args.kd
    .uniform_work_group_size: 1
    .uses_dynamic_stack: false
    .vgpr_count:     256
    .vgpr_spill_count: 0
    .wavefront_size: 64
